# baseline (speedup 1.0000x reference)
.Lq_noprio:
	s_waitcnt vmcnt(12)
	v_cvt_pk_f16_f32 v164, v36, v40
	v_cvt_pk_f16_f32 v180, v68, v72
	v_pk_add_f16 v164, v164, -0.5 op_sel_hi:[1,0]
	v_pk_add_f16 v180, v180, -0.5 op_sel_hi:[1,0]
	v_pk_mul_f16 v196, v180, v180
	v_pk_mul_f16 v212, v164, v180
	v_pk_fma_f16 v196, v164, v164, v196
	v_cvt_pk_f16_f32 v168, v37, v41
	v_cvt_pk_f16_f32 v184, v69, v73
	v_pk_add_f16 v168, v168, -0.5 op_sel_hi:[1,0]
	v_pk_add_f16 v184, v184, -0.5 op_sel_hi:[1,0]
	v_pk_mul_f16 v200, v184, v184
	v_pk_mul_f16 v216, v168, v184
	v_pk_fma_f16 v200, v168, v168, v200
	v_cvt_pk_f16_f32 v172, v38, v42
	v_cvt_pk_f16_f32 v188, v70, v74
	v_pk_add_f16 v172, v172, -0.5 op_sel_hi:[1,0]
	v_pk_add_f16 v188, v188, -0.5 op_sel_hi:[1,0]
	v_pk_mul_f16 v204, v188, v188
	v_pk_mul_f16 v220, v172, v188
	v_pk_fma_f16 v204, v172, v172, v204
	v_cvt_pk_f16_f32 v176, v39, v43
	v_cvt_pk_f16_f32 v192, v71, v75
	v_pk_add_f16 v176, v176, -0.5 op_sel_hi:[1,0]
	v_pk_add_f16 v192, v192, -0.5 op_sel_hi:[1,0]
	v_pk_mul_f16 v208, v192, v192
	v_pk_mul_f16 v224, v176, v192
	v_pk_fma_f16 v208, v176, v176, v208
	s_waitcnt vmcnt(8)
	v_cvt_pk_f16_f32 v165, v44, v48
	v_cvt_pk_f16_f32 v181, v76, v80
	v_pk_add_f16 v165, v165, -0.5 op_sel_hi:[1,0]
	v_pk_add_f16 v181, v181, -0.5 op_sel_hi:[1,0]
	v_pk_mul_f16 v197, v181, v181
	v_pk_mul_f16 v213, v165, v181
	v_pk_fma_f16 v197, v165, v165, v197
	v_cvt_pk_f16_f32 v169, v45, v49
	v_cvt_pk_f16_f32 v185, v77, v81
	v_pk_add_f16 v169, v169, -0.5 op_sel_hi:[1,0]
	v_pk_add_f16 v185, v185, -0.5 op_sel_hi:[1,0]
	v_pk_mul_f16 v201, v185, v185
	v_pk_mul_f16 v217, v169, v185
	v_pk_fma_f16 v201, v169, v169, v201
	v_cvt_pk_f16_f32 v173, v46, v50
	v_cvt_pk_f16_f32 v189, v78, v82
	v_pk_add_f16 v173, v173, -0.5 op_sel_hi:[1,0]
	v_pk_add_f16 v189, v189, -0.5 op_sel_hi:[1,0]
	v_pk_mul_f16 v205, v189, v189
	v_pk_mul_f16 v221, v173, v189
	v_pk_fma_f16 v205, v173, v173, v205
	v_cvt_pk_f16_f32 v177, v47, v51
	v_cvt_pk_f16_f32 v193, v79, v83
	v_pk_add_f16 v177, v177, -0.5 op_sel_hi:[1,0]
	v_pk_add_f16 v193, v193, -0.5 op_sel_hi:[1,0]
	v_pk_mul_f16 v209, v193, v193
	v_pk_mul_f16 v225, v177, v193
	v_pk_fma_f16 v209, v177, v177, v209
	s_waitcnt vmcnt(4)
	v_cvt_pk_f16_f32 v166, v52, v56
	v_cvt_pk_f16_f32 v182, v84, v88
	v_pk_add_f16 v166, v166, -0.5 op_sel_hi:[1,0]
	v_pk_add_f16 v182, v182, -0.5 op_sel_hi:[1,0]
	v_pk_mul_f16 v198, v182, v182
	v_pk_mul_f16 v214, v166, v182
	v_pk_fma_f16 v198, v166, v166, v198
	v_cvt_pk_f16_f32 v170, v53, v57
	v_cvt_pk_f16_f32 v186, v85, v89
	v_pk_add_f16 v170, v170, -0.5 op_sel_hi:[1,0]
	v_pk_add_f16 v186, v186, -0.5 op_sel_hi:[1,0]
	v_pk_mul_f16 v202, v186, v186
	v_pk_mul_f16 v218, v170, v186
	v_pk_fma_f16 v202, v170, v170, v202
	v_cvt_pk_f16_f32 v174, v54, v58
	v_cvt_pk_f16_f32 v190, v86, v90
	v_pk_add_f16 v174, v174, -0.5 op_sel_hi:[1,0]
	v_pk_add_f16 v190, v190, -0.5 op_sel_hi:[1,0]
	v_pk_mul_f16 v206, v190, v190
	v_pk_mul_f16 v222, v174, v190
	v_pk_fma_f16 v206, v174, v174, v206
	v_cvt_pk_f16_f32 v178, v55, v59
	v_cvt_pk_f16_f32 v194, v87, v91
	v_pk_add_f16 v178, v178, -0.5 op_sel_hi:[1,0]
	v_pk_add_f16 v194, v194, -0.5 op_sel_hi:[1,0]
	v_pk_mul_f16 v210, v194, v194
	v_pk_mul_f16 v226, v178, v194
	v_pk_fma_f16 v210, v178, v178, v210
	s_waitcnt vmcnt(0)
	global_load_dwordx4 v[100:103], v240, s[18:19] offset:0 sc1 nt
	global_load_dwordx4 v[104:107], v240, s[18:19] offset:2048 sc1 nt
	global_load_dwordx4 v[132:135], v240, s[20:21] offset:0 sc1 nt
	global_load_dwordx4 v[136:139], v240, s[20:21] offset:2048 sc1 nt
	global_load_dwordx4 v[108:111], v241, s[18:19] offset:0 sc1 nt
	global_load_dwordx4 v[112:115], v241, s[18:19] offset:2048 sc1 nt
	global_load_dwordx4 v[140:143], v241, s[20:21] offset:0 sc1 nt
	global_load_dwordx4 v[144:147], v241, s[20:21] offset:2048 sc1 nt
	global_load_dwordx4 v[116:119], v242, s[18:19] offset:0 sc1 nt
	global_load_dwordx4 v[120:123], v242, s[18:19] offset:2048 sc1 nt
	global_load_dwordx4 v[148:151], v242, s[20:21] offset:0 sc1 nt
	global_load_dwordx4 v[152:155], v242, s[20:21] offset:2048 sc1 nt
	global_load_dwordx4 v[124:127], v243, s[18:19] offset:0 sc1 nt
	global_load_dwordx4 v[128:131], v243, s[18:19] offset:2048 sc1 nt
	global_load_dwordx4 v[156:159], v243, s[20:21] offset:0 sc1 nt
	global_load_dwordx4 v[160:163], v243, s[20:21] offset:2048 sc1 nt
	v_cvt_pk_f16_f32 v167, v60, v64
	v_cvt_pk_f16_f32 v183, v92, v96
	v_pk_add_f16 v167, v167, -0.5 op_sel_hi:[1,0]
	v_pk_add_f16 v183, v183, -0.5 op_sel_hi:[1,0]
	v_pk_mul_f16 v199, v183, v183
	v_pk_mul_f16 v215, v167, v183
	v_pk_fma_f16 v199, v167, v167, v199
	v_cvt_pk_f16_f32 v171, v61, v65
	v_cvt_pk_f16_f32 v187, v93, v97
	v_pk_add_f16 v171, v171, -0.5 op_sel_hi:[1,0]
	v_pk_add_f16 v187, v187, -0.5 op_sel_hi:[1,0]
	v_pk_mul_f16 v203, v187, v187
	v_pk_mul_f16 v219, v171, v187
	v_pk_fma_f16 v203, v171, v171, v203
	v_cvt_pk_f16_f32 v175, v62, v66
	v_cvt_pk_f16_f32 v191, v94, v98
	v_pk_add_f16 v175, v175, -0.5 op_sel_hi:[1,0]
	v_pk_add_f16 v191, v191, -0.5 op_sel_hi:[1,0]
	v_pk_mul_f16 v207, v191, v191
	v_pk_mul_f16 v223, v175, v191
	v_pk_fma_f16 v207, v175, v175, v207
	v_cvt_pk_f16_f32 v179, v63, v67
	v_cvt_pk_f16_f32 v195, v95, v99
	v_pk_add_f16 v179, v179, -0.5 op_sel_hi:[1,0]
	v_pk_add_f16 v195, v195, -0.5 op_sel_hi:[1,0]
	v_pk_mul_f16 v211, v195, v195
	v_pk_mul_f16 v227, v179, v195
	v_pk_fma_f16 v211, v179, v179, v211
	v_mfma_f32_16x16x32_f16 v[68:71], v[164:167], v[24:27], 0
	v_mfma_f32_16x16x32_f16 v[72:75], v[168:171], v[24:27], 0
	v_mfma_f32_16x16x32_f16 v[76:79], v[172:175], v[24:27], 0
	v_mfma_f32_16x16x32_f16 v[80:83], v[176:179], v[24:27], 0
	v_mfma_f32_16x16x32_f16 v[84:87], v[180:183], v[24:27], 0
	v_mfma_f32_16x16x32_f16 v[88:91], v[184:187], v[24:27], 0
	v_mfma_f32_16x16x32_f16 v[92:95], v[188:191], v[24:27], 0
	v_mfma_f32_16x16x32_f16 v[96:99], v[192:195], v[24:27], 0
	s_nop 1
	v_cvt_pk_f16_f32 v36, v68, v72
	s_nop 0
	v_cvt_pk_f16_f32 v37, v76, v80
	v_cvt_pk_f16_f32 v38, v69, v73
	v_cvt_pk_f16_f32 v39, v77, v81
	v_cvt_pk_f16_f32 v40, v70, v74
	v_cvt_pk_f16_f32 v41, v78, v82
	v_cvt_pk_f16_f32 v42, v71, v75
	v_cvt_pk_f16_f32 v43, v79, v83
	v_mfma_f32_16x16x32_f16 v[68:71], v[196:199], v[24:27], 0
	v_mfma_f32_16x16x32_f16 v[72:75], v[200:203], v[24:27], 0
	v_mfma_f32_16x16x32_f16 v[76:79], v[204:207], v[24:27], 0
	v_mfma_f32_16x16x32_f16 v[80:83], v[208:211], v[24:27], 0
	v_cvt_pk_f16_f32 v44, v84, v88
	v_cvt_pk_f16_f32 v45, v92, v96
	v_cvt_pk_f16_f32 v46, v85, v89
	v_cvt_pk_f16_f32 v47, v93, v97
	v_cvt_pk_f16_f32 v48, v86, v90
	v_cvt_pk_f16_f32 v49, v94, v98
	v_cvt_pk_f16_f32 v50, v87, v91
	v_cvt_pk_f16_f32 v51, v95, v99
	v_mfma_f32_16x16x32_f16 v[84:87], v[212:215], v[24:27], 0
	v_mfma_f32_16x16x32_f16 v[88:91], v[216:219], v[24:27], 0
	v_mfma_f32_16x16x32_f16 v[92:95], v[220:223], v[24:27], 0
	v_mfma_f32_16x16x32_f16 v[96:99], v[224:227], v[24:27], 0
	v_cvt_pk_f16_f32 v52, v68, v72
	v_cvt_pk_f16_f32 v53, v76, v80
	v_cvt_pk_f16_f32 v54, v69, v73
	v_cvt_pk_f16_f32 v55, v77, v81
	v_cvt_pk_f16_f32 v56, v70, v74
	v_cvt_pk_f16_f32 v57, v78, v82
	v_cvt_pk_f16_f32 v58, v71, v75
	v_cvt_pk_f16_f32 v59, v79, v83
	v_cvt_pk_f16_f32 v60, v84, v88
	v_cvt_pk_f16_f32 v61, v92, v96
	v_cvt_pk_f16_f32 v62, v85, v89
	v_cvt_pk_f16_f32 v63, v93, v97
	v_cvt_pk_f16_f32 v64, v86, v90
	v_cvt_pk_f16_f32 v65, v94, v98
	v_cvt_pk_f16_f32 v66, v87, v91
	v_cvt_pk_f16_f32 v67, v95, v99
	s_mov_b64 exec, s[38:39]
	ds_write_b128 v4, v[40:43] offset:0
	ds_write_b128 v4, v[48:51] offset:512
	ds_write_b128 v4, v[56:59] offset:1024
	ds_write_b128 v4, v[64:67] offset:1536
	s_mov_b64 exec, -1
	v_mfma_f32_16x16x32_f16 v[68:71], v[24:27], v[36:39], 0
	v_mfma_f32_16x16x32_f16 v[72:75], v[24:27], v[44:47], 0
	v_mfma_f32_16x16x32_f16 v[76:79], v[24:27], v[52:55], v[0:3]
	v_mfma_f32_16x16x32_f16 v[80:83], v[24:27], v[60:63], 0
	v_mfma_f32_16x16x32_f16 v[84:87], v[28:31], v[36:39], 0
	v_mfma_f32_16x16x32_f16 v[88:91], v[28:31], v[44:47], 0
	v_mfma_f32_16x16x32_f16 v[92:95], v[28:31], v[52:55], v[0:3]
	v_mfma_f32_16x16x32_f16 v[96:99], v[28:31], v[60:63], 0
	v_mfma_f32_16x16x32_f16 v[84:87], v[32:35], v[40:43], v[84:87]
	v_mfma_f32_16x16x32_f16 v[88:91], v[32:35], v[48:51], v[88:91]
	v_mfma_f32_16x16x32_f16 v[92:95], v[32:35], v[56:59], v[92:95]
	v_mfma_f32_16x16x32_f16 v[96:99], v[32:35], v[64:67], v[96:99]
	s_waitcnt lgkmcnt(0)
	ds_write_b32 v6, v6 offset:0
	ds_read_b32 v9, v7 offset:0
	v_mul_f32_e32 v244, v68, v72
	v_mul_f32_e32 v250, v69, v73
	v_mul_f32_e64 v245, -v72, v72
	v_mul_f32_e64 v251, -v73, v73
	v_add_f32_e32 v246, v68, v72
	v_add_f32_e32 v252, v69, v73
	v_fma_f32 v245, -v68, v68, v245
	v_fma_f32 v251, -v69, v69, v251
	v_fma_f32 v247, v10, v246, v11
	v_fma_f32 v253, v10, v252, v11
	v_fma_f32 v246, v13, v80, v14
	v_fma_f32 v252, v13, v81, v14
	v_fma_f32 v248, v12, v76, v245
	v_fma_f32 v254, v12, v77, v251
	v_fma_f32 v249, 2.0, v244, v247
	v_fma_f32 v255, 2.0, v250, v253
	v_sub_f32_e32 v247, v247, v245
	v_sub_f32_e32 v253, v253, v251
	v_fma_f32 v246, -2.0, v244, v246
	v_fma_f32 v252, -2.0, v250, v252
	v_mul_f32_e32 v247, v247, v248
	v_mul_f32_e32 v253, v253, v254
	v_rcp_f32_e32 v247, v247
	v_rcp_f32_e32 v253, v253
	v_mul_f32_e32 v249, v249, v246
	v_mul_f32_e32 v255, v255, v252
	v_fma_f32 v19, v249, v247, v19
	v_fma_f32 v19, v255, v253, v19
	v_mul_f32_e32 v244, v70, v74
	v_mul_f32_e32 v250, v71, v75
	v_mul_f32_e64 v245, -v74, v74
	v_mul_f32_e64 v251, -v75, v75
	v_add_f32_e32 v246, v70, v74
	v_add_f32_e32 v252, v71, v75
	v_fma_f32 v245, -v70, v70, v245
	v_fma_f32 v251, -v71, v71, v251
	v_fma_f32 v247, v10, v246, v11
	v_fma_f32 v253, v10, v252, v11
	v_fma_f32 v246, v13, v82, v14
	v_fma_f32 v252, v13, v83, v14
	v_fma_f32 v248, v12, v78, v245
	v_fma_f32 v254, v12, v79, v251
	v_fma_f32 v249, 2.0, v244, v247
	v_fma_f32 v255, 2.0, v250, v253
	v_sub_f32_e32 v247, v247, v245
	v_sub_f32_e32 v253, v253, v251
	v_fma_f32 v246, -2.0, v244, v246
	v_fma_f32 v252, -2.0, v250, v252
	v_mul_f32_e32 v247, v247, v248
	v_mul_f32_e32 v253, v253, v254
	v_rcp_f32_e32 v247, v247
	v_rcp_f32_e32 v253, v253
	v_mul_f32_e32 v249, v249, v246
	v_mul_f32_e32 v255, v255, v252
	v_fma_f32 v20, v249, v247, v20
	v_fma_f32 v20, v255, v253, v20
	v_mfma_f32_16x16x32_f16 v[68:71], v[24:27], v[40:43], 0
	v_mfma_f32_16x16x32_f16 v[72:75], v[24:27], v[48:51], 0
	v_mfma_f32_16x16x32_f16 v[76:79], v[24:27], v[56:59], v[0:3]
	v_mfma_f32_16x16x32_f16 v[80:83], v[24:27], v[64:67], 0
	s_waitcnt lgkmcnt(0)
	v_cmp_ne_u32_e32 vcc, 0, v9
	s_cbranch_vccnz .Lq_go_0
